# speedup vs baseline: 1.0894x; 1.0009x over previous
.LBB2_93:
	ds_read_b128 v[18:21], v125 offset:8192
	ds_read_b128 v[34:37], v125 offset:9216
	v_cvt_pkrtz_f16_f32 v50, v74, v75
	v_cvt_pkrtz_f16_f32 v51, v76, v77
	v_cvt_pkrtz_f16_f32 v52, v82, v83
	v_cvt_pkrtz_f16_f32 v53, v84, v85
	v_cvt_pkrtz_f16_f32 v62, v86, v87
	v_cvt_pkrtz_f16_f32 v63, v88, v89
	v_cvt_pkrtz_f16_f32 v64, v94, v95
	s_waitcnt lgkmcnt(0)
	v_mfma_f32_32x32x16_f16 v[18:33], v[18:21], v[50:53], 0
	v_cvt_pkrtz_f16_f32 v65, v110, v111
	ds_read_b128 v[38:41], v125 offset:10240
	v_cvt_pkrtz_f16_f32 v78, v108, v109
	v_cvt_pkrtz_f16_f32 v79, v106, v107
	v_cvt_pkrtz_f16_f32 v80, v104, v105
	v_cvt_pkrtz_f16_f32 v81, v100, v101
	s_add_i32 s0, 0, 0x1a800
	v_mfma_f32_32x32x16_f16 v[18:33], v[34:37], v[62:65], v[18:33]
	v_lshl_add_u32 v99, v165, 1, s0
	ds_read_b128 v[2:5], v125
	ds_read_b128 v[58:61], v125 offset:1024
	ds_read_b128 v[120:123], v125 offset:2048
	ds_read_b128 v[174:177], v125 offset:3072
	ds_read_b128 v[178:181], v125 offset:4096
	ds_read_b128 v[182:185], v125 offset:5120
	ds_read_b128 v[34:37], v125 offset:11264
	ds_read_b128 v[186:189], v125 offset:6144
	ds_read_b128 v[190:193], v125 offset:7168
	v_cvt_pkrtz_f16_f32 v114, v96, v97
	v_cvt_pkrtz_f16_f32 v115, v92, v93
	s_waitcnt lgkmcnt(0)
	v_mfma_f32_32x32x16_f16 v[18:33], v[38:41], v[78:81], v[18:33]
	ds_read_b128 v[194:197], v99 offset:11648
	ds_read_b128 v[198:201], v99 offset:11936
	ds_read_b128 v[38:41], v125 offset:12288
	v_cvt_pkrtz_f16_f32 v116, v90, v91
	v_cvt_pkrtz_f16_f32 v117, v102, v103
	ds_read_b128 v[202:205], v99 offset:12224
	ds_read_b128 v[206:209], v99 offset:12512
	ds_read_b128 v[210:213], v99 offset:12800
	ds_read_b128 v[54:57], v99 offset:13088
	ds_read_b128 v[70:73], v99 offset:13376
	ds_read_b128 v[66:69], v99 offset:13664
	ds_read_b128 v[214:217], v125 offset:13312
	ds_read_b128 v[218:221], v99 offset:13952
	ds_read_b128 v[222:225], v125 offset:14336
	ds_read_b128 v[226:229], v125 offset:15360
	ds_read_b128 v[230:233], v99 offset:14240
	s_mov_b32 s16, 0xff61b1e6
	s_mov_b32 s17, 0
	v_mfma_f32_32x32x16_f16 v[18:33], v[34:37], v[114:117], v[18:33]
	s_waitcnt lgkmcnt(0)
	v_mfma_f32_32x32x16_f16 v[34:49], v[38:41], v[50:53], 0
	s_nop 9
	v_add_f32_e32 v112, v18, v218
	v_add_f32_e32 v113, v19, v219
	v_add_f32_e32 v159, v20, v220
	v_add_f32_e32 v161, v21, v221
	ds_read_b128 v[18:21], v99 offset:14528
	v_add_f32_e32 v164, v22, v230
	v_add_f32_e32 v165, v23, v231
	v_mfma_f32_32x32x16_f16 v[34:49], v[214:217], v[62:65], v[34:49]
	v_add_f32_e32 v170, v24, v232
	v_add_f32_e32 v173, v25, v233
	ds_read_b128 v[22:25], v99 offset:14816
	s_waitcnt lgkmcnt(0)
	v_add_f32_e32 v26, v26, v18
	v_add_f32_e32 v27, v27, v19
	v_add_f32_e32 v28, v28, v20
	v_add_f32_e32 v29, v29, v21
	v_mfma_f32_32x32x16_f16 v[34:49], v[222:225], v[78:81], v[34:49]
	ds_read_b128 v[18:21], v99 offset:15104
	v_add_f32_e32 v30, v30, v22
	v_add_f32_e32 v31, v31, v23
	v_add_f32_e32 v32, v32, v24
	v_add_f32_e32 v33, v33, v25
	ds_read_b128 v[22:25], v99 offset:15392
	v_mfma_f32_32x32x16_f16 v[34:49], v[226:229], v[114:117], v[34:49]
	v_mfma_f32_32x32x16_f16 v[2:17], v[2:5], v[50:53], 0
	s_waitcnt lgkmcnt(0)
	s_nop 9
	v_add_f32_e32 v34, v34, v18
	v_add_f32_e32 v35, v35, v19
	v_add_f32_e32 v36, v36, v20
	v_add_f32_e32 v37, v37, v21
	ds_read_b128 v[18:21], v99 offset:15680
	v_add_f32_e32 v38, v38, v22
	v_add_f32_e32 v39, v39, v23
	v_add_f32_e32 v40, v40, v24
	v_add_f32_e32 v41, v41, v25
	ds_read_b128 v[22:25], v99 offset:15968
	s_waitcnt lgkmcnt(0)
	v_add_f32_e32 v42, v42, v18
	v_add_f32_e32 v43, v43, v19
	v_add_f32_e32 v44, v44, v20
	v_add_f32_e32 v45, v45, v21
	v_cvt_pkrtz_f16_f32 v18, v112, v113
	v_cvt_pkrtz_f16_f32 v19, v159, v161
	v_cvt_pkrtz_f16_f32 v20, v164, v165
	v_cvt_pkrtz_f16_f32 v21, v170, v173
	ds_write_b128 v166, v[18:21]
	v_cvt_pkrtz_f16_f32 v18, v26, v27
	v_cvt_pkrtz_f16_f32 v19, v28, v29
	v_cvt_pkrtz_f16_f32 v20, v30, v31
	v_cvt_pkrtz_f16_f32 v21, v32, v33
	v_add_f32_e32 v22, v46, v22
	v_add_f32_e32 v23, v47, v23
	v_add_f32_e32 v24, v48, v24
	v_add_f32_e32 v25, v49, v25
	ds_write_b128 v166, v[18:21] offset:32
	v_cvt_pkrtz_f16_f32 v18, v34, v35
	v_cvt_pkrtz_f16_f32 v19, v36, v37
	v_cvt_pkrtz_f16_f32 v20, v38, v39
	v_cvt_pkrtz_f16_f32 v21, v40, v41
	ds_write_b128 v166, v[18:21] offset:64
	v_cvt_pkrtz_f16_f32 v18, v42, v43
	v_cvt_pkrtz_f16_f32 v19, v44, v45
	v_cvt_pkrtz_f16_f32 v20, v22, v23
	v_cvt_pkrtz_f16_f32 v21, v24, v25
	ds_write_b128 v166, v[18:21] offset:96
	ds_read_b128 v[18:21], v125 offset:16384
	ds_read_b128 v[22:25], v125 offset:17408
	s_waitcnt lgkmcnt(0)
	v_mfma_f32_32x32x16_f16 v[30:45], v[50:53], v[18:21], 0
	v_add_u32_e32 v112, v167, v162
	v_add_u32_e32 v159, v171, v172
	v_mfma_f32_32x32x16_f16 v[2:17], v[58:61], v[62:65], v[2:17]
	v_mfma_f32_32x32x16_f16 v[30:45], v[62:65], v[22:25], v[30:45]
	ds_read_b128 v[18:21], v125 offset:18432
	ds_read_b128 v[22:25], v125 offset:19456
	v_mfma_f32_32x32x16_f16 v[2:17], v[120:123], v[78:81], v[2:17]
	s_waitcnt lgkmcnt(0)
	v_mfma_f32_32x32x16_f16 v[30:45], v[78:81], v[18:21], v[30:45]
	v_add3_u32 v18, s0, v168, v160
	ds_read_b32 v46, v18 offset:16256
	v_mfma_f32_32x32x16_f16 v[2:17], v[174:177], v[114:117], v[2:17]
	v_mfma_f32_32x32x16_f16 v[30:45], v[114:117], v[22:25], v[30:45]
	s_nop 10
	v_fmamk_f32 v58, v194, 0x3e38aa3b, v2
	v_fmamk_f32 v59, v195, 0x3e38aa3b, v3
	v_fmamk_f32 v99, v198, 0x3e38aa3b, v6
	v_fmamk_f32 v113, v202, 0x3e38aa3b, v10
	v_fmamk_f32 v120, v203, 0x3e38aa3b, v11
	v_fmamk_f32 v121, v204, 0x3e38aa3b, v12
	v_fmamk_f32 v122, v205, 0x3e38aa3b, v13
	s_waitcnt lgkmcnt(0)
	v_add_f32_e32 v2, v46, v30
	v_add_f32_e32 v3, v46, v31
	v_add_f32_e32 v47, v46, v32
	v_add_f32_e32 v48, v46, v33
	v_add_f32_e32 v49, v46, v34
	v_add_f32_e32 v60, v46, v35
	v_add_f32_e32 v61, v46, v36
	v_add_f32_e32 v37, v46, v37
	v_add_f32_e32 v38, v46, v38
	v_add_f32_e32 v39, v46, v39
	v_add_f32_e32 v40, v46, v40
	v_add_f32_e32 v41, v46, v41
	v_add_f32_e32 v42, v46, v42
	v_add_f32_e32 v43, v46, v43
	v_add_f32_e32 v44, v46, v44
	v_add_f32_e32 v45, v46, v45
	v_cvt_pkrtz_f16_f32 v34, v2, v3
	v_cvt_pkrtz_f16_f32 v35, v47, v48
	v_cvt_pkrtz_f16_f32 v36, v49, v60
	v_cvt_pkrtz_f16_f32 v37, v61, v37
	ds_write_b128 v112, v[34:37]
	v_cvt_pkrtz_f16_f32 v34, v38, v39
	v_cvt_pkrtz_f16_f32 v35, v40, v41
	v_cvt_pkrtz_f16_f32 v36, v42, v43
	v_cvt_pkrtz_f16_f32 v37, v44, v45
	ds_write_b128 v112, v[34:37] offset:32
	ds_read_b128 v[34:37], v125 offset:20480
	v_fmamk_f32 v60, v196, 0x3e38aa3b, v4
	v_fmamk_f32 v61, v197, 0x3e38aa3b, v5
	ds_read_b128 v[2:5], v125 offset:21504
	s_waitcnt lgkmcnt(0)
	v_mfma_f32_32x32x16_f16 v[34:49], v[50:53], v[34:37], 0
	v_fmamk_f32 v14, v206, 0x3e38aa3b, v14
	v_fmamk_f32 v15, v207, 0x3e38aa3b, v15
	v_fmamk_f32 v16, v208, 0x3e38aa3b, v16
	v_fmac_f32_e32 v17, 0x3e38aa3b, v209
	v_mfma_f32_32x32x16_f16 v[34:49], v[62:65], v[2:5], v[34:49]
	ds_read_b128 v[2:5], v125 offset:22528
	v_mfma_f32_32x32x16_f16 v[18:33], v[178:181], v[50:53], 0
	v_fmamk_f32 v50, v199, 0x3e38aa3b, v7
	v_fmamk_f32 v51, v200, 0x3e38aa3b, v8
	v_fmamk_f32 v52, v201, 0x3e38aa3b, v9
	ds_read_b128 v[6:9], v125 offset:23552
	s_waitcnt lgkmcnt(0)
	v_mfma_f32_32x32x16_f16 v[34:49], v[78:81], v[2:5], v[34:49]
	v_add3_u32 v2, s0, v169, v160
	ds_read_b32 v2, v2 offset:16256
	s_lshl_b32 s0, s28, 9
	s_add_i32 s0, s0, 0
	s_add_i32 s14, s0, 0x27800
	v_mfma_f32_32x32x16_f16 v[18:33], v[182:185], v[62:65], v[18:33]
	v_mfma_f32_32x32x16_f16 v[34:49], v[114:117], v[6:9], v[34:49]
	v_mfma_f32_32x32x16_f16 v[18:33], v[186:189], v[78:81], v[18:33]
	s_waitcnt lgkmcnt(0)
	s_nop 9
	v_add_f32_e32 v3, v2, v34
	v_add_f32_e32 v4, v2, v35
	v_add_f32_e32 v5, v2, v36
	v_add_f32_e32 v6, v2, v37
	v_add_f32_e32 v7, v2, v38
	v_add_f32_e32 v8, v2, v39
	v_add_f32_e32 v9, v2, v40
	v_add_f32_e32 v10, v2, v41
	v_add_f32_e32 v11, v2, v42
	v_add_f32_e32 v12, v2, v43
	v_add_f32_e32 v13, v2, v44
	v_add_f32_e32 v34, v2, v45
	v_add_f32_e32 v35, v2, v46
	v_add_f32_e32 v36, v2, v47
	v_add_f32_e32 v37, v2, v48
	v_add_f32_e32 v38, v2, v49
	v_cvt_pkrtz_f16_f32 v2, v3, v4
	v_cvt_pkrtz_f16_f32 v3, v5, v6
	v_cvt_pkrtz_f16_f32 v4, v7, v8
	v_cvt_pkrtz_f16_f32 v5, v9, v10
	ds_write_b128 v112, v[2:5] offset:8704
	v_cvt_pkrtz_f16_f32 v2, v11, v12
	v_cvt_pkrtz_f16_f32 v3, v13, v34
	v_cvt_pkrtz_f16_f32 v4, v35, v36
	v_cvt_pkrtz_f16_f32 v5, v37, v38
	ds_write_b128 v112, v[2:5] offset:8736
	s_nop 0
	s_waitcnt lgkmcnt(0)
	s_barrier
	ds_read_b128 v[2:5], v159
	ds_read_b128 v[10:13], v159 offset:32
	v_mfma_f32_32x32x16_f16 v[18:33], v[190:193], v[114:117], v[18:33]
	v_cvt_pkrtz_f16_f32 v6, v58, v59
	v_cvt_pkrtz_f16_f32 v7, v60, v61
	v_cvt_pkrtz_f16_f32 v8, v99, v50
	v_cvt_pkrtz_f16_f32 v9, v51, v52
	v_cvt_pkrtz_f16_f32 v78, v113, v120
	v_cvt_pkrtz_f16_f32 v79, v121, v122
	v_cvt_pkrtz_f16_f32 v80, v14, v15
	s_nop 4
	v_fmamk_f32 v22, v54, 0x3e38aa3b, v22
	v_fmamk_f32 v23, v55, 0x3e38aa3b, v23
	v_fmamk_f32 v24, v56, 0x3e38aa3b, v24
	v_fmamk_f32 v25, v57, 0x3e38aa3b, v25
	s_waitcnt lgkmcnt(1)
	v_mfma_f32_32x32x16_f16 v[50:65], v[2:5], v[6:9], 0
	v_cvt_pkrtz_f16_f32 v81, v16, v17
	ds_read_b128 v[2:5], v159 offset:64
	v_fmamk_f32 v18, v210, 0x3e38aa3b, v18
	v_fmamk_f32 v19, v211, 0x3e38aa3b, v19
	v_fmamk_f32 v20, v212, 0x3e38aa3b, v20
	v_fmamk_f32 v21, v213, 0x3e38aa3b, v21
	v_fmamk_f32 v26, v70, 0x3e38aa3b, v26
	s_waitcnt lgkmcnt(1)
	v_mfma_f32_32x32x16_f16 v[50:65], v[10:13], v[78:81], v[50:65]
	v_fmamk_f32 v27, v71, 0x3e38aa3b, v27
	v_fmamk_f32 v28, v72, 0x3e38aa3b, v28
	v_fmamk_f32 v14, v73, 0x3e38aa3b, v29
	v_cvt_pkrtz_f16_f32 v70, v18, v19
	v_cvt_pkrtz_f16_f32 v71, v20, v21
	v_cvt_pkrtz_f16_f32 v72, v22, v23
	v_cvt_pkrtz_f16_f32 v73, v24, v25
	ds_read_b128 v[10:13], v159 offset:96
	v_fmamk_f32 v15, v66, 0x3e38aa3b, v30
	s_waitcnt lgkmcnt(1)
	v_mfma_f32_32x32x16_f16 v[50:65], v[2:5], v[70:73], v[50:65]
	v_fmamk_f32 v2, v67, 0x3e38aa3b, v31
	v_fmamk_f32 v3, v68, 0x3e38aa3b, v32
	v_fmac_f32_e32 v33, 0x3e38aa3b, v69
	v_cvt_pkrtz_f16_f32 v66, v26, v27
	v_cvt_pkrtz_f16_f32 v67, v28, v14
	v_cvt_pkrtz_f16_f32 v68, v15, v2
	v_cvt_pkrtz_f16_f32 v69, v3, v33
	v_add_u32_e32 v113, v163, v162
	s_waitcnt lgkmcnt(0)
	v_mfma_f32_32x32x16_f16 v[50:65], v[10:13], v[66:69], v[50:65]
	ds_read_b128 v[2:5], v159 offset:4608
	ds_read_b128 v[10:13], v159 offset:4640
	s_waitcnt lgkmcnt(1)
	v_mfma_f32_32x32x16_f16 v[34:49], v[2:5], v[6:9], 0
	s_waitcnt lgkmcnt(0)
	v_mfma_f32_32x32x16_f16 v[34:49], v[10:13], v[78:81], v[34:49]
	ds_read_b128 v[2:5], v159 offset:4672
	ds_read_b128 v[10:13], v159 offset:4704
	s_waitcnt lgkmcnt(1)
	v_mfma_f32_32x32x16_f16 v[34:49], v[2:5], v[70:73], v[34:49]
	s_waitcnt lgkmcnt(0)
	v_mfma_f32_32x32x16_f16 v[34:49], v[10:13], v[66:69], v[34:49]
	ds_read_b128 v[2:5], v159 offset:9216
	ds_read_b128 v[10:13], v159 offset:9248
	s_waitcnt lgkmcnt(1)
	v_mfma_f32_32x32x16_f16 v[18:33], v[2:5], v[6:9], 0
	s_waitcnt lgkmcnt(0)
	v_mfma_f32_32x32x16_f16 v[18:33], v[10:13], v[78:81], v[18:33]
	ds_read_b128 v[2:5], v159 offset:9280
	ds_read_b128 v[10:13], v159 offset:9312
	s_waitcnt lgkmcnt(1)
	v_mfma_f32_32x32x16_f16 v[18:33], v[2:5], v[70:73], v[18:33]
	ds_read_b128 v[2:5], v159 offset:13824
	ds_read_b128 v[114:117], v159 offset:13856
	ds_read_b128 v[120:123], v159 offset:13888
	ds_read_b128 v[164:167], v159 offset:13920
	s_waitcnt lgkmcnt(4)
	v_mfma_f32_32x32x16_f16 v[18:33], v[10:13], v[66:69], v[18:33]
	s_waitcnt lgkmcnt(3)
	v_mfma_f32_32x32x16_f16 v[2:17], v[2:5], v[6:9], 0
	s_waitcnt lgkmcnt(2)
	v_mfma_f32_32x32x16_f16 v[2:17], v[114:117], v[78:81], v[2:17]
	s_waitcnt lgkmcnt(1)
	v_mfma_f32_32x32x16_f16 v[2:17], v[120:123], v[70:73], v[2:17]
	s_waitcnt lgkmcnt(0)
	v_mfma_f32_32x32x16_f16 v[2:17], v[164:167], v[66:69], v[2:17]
	v_mov_b32_e32 v99, 0
	s_nop 10
	s_nop 1
	v_exp_f32_e32 v34, v34
	v_exp_f32_e32 v35, v35
	v_exp_f32_e32 v36, v36
	v_exp_f32_e32 v37, v37
	v_cvt_pkrtz_f16_f32 v34, v34, v35
	v_cvt_pkrtz_f16_f32 v35, v36, v37
	v_exp_f32_e32 v36, v38
	v_exp_f32_e32 v37, v39
	v_exp_f32_e32 v38, v40
	v_exp_f32_e32 v39, v41
	v_exp_f32_e32 v40, v42
	v_exp_f32_e32 v41, v43
	v_exp_f32_e32 v42, v44
	v_exp_f32_e32 v43, v45
	v_cvt_pkrtz_f16_f32 v36, v36, v37
	v_cvt_pkrtz_f16_f32 v37, v38, v39
	v_cvt_pkrtz_f16_f32 v38, v40, v41
	v_cvt_pkrtz_f16_f32 v39, v42, v43
	v_exp_f32_e32 v40, v46
	v_exp_f32_e32 v41, v47
	v_exp_f32_e32 v42, v48
	v_exp_f32_e32 v43, v49
	v_exp_f32_e32 v18, v18
	v_exp_f32_e32 v19, v19
	v_exp_f32_e32 v20, v20
	v_exp_f32_e32 v21, v21
	v_exp_f32_e32 v50, v50
	v_exp_f32_e32 v51, v51
	v_exp_f32_e32 v52, v52
	v_exp_f32_e32 v53, v53
	v_cvt_pkrtz_f16_f32 v40, v40, v41
	v_cvt_pkrtz_f16_f32 v41, v42, v43
	v_cvt_pkrtz_f16_f32 v42, v18, v19
	v_cvt_pkrtz_f16_f32 v43, v20, v21
	v_exp_f32_e32 v18, v22
	v_exp_f32_e32 v19, v23
	v_exp_f32_e32 v20, v24
	v_exp_f32_e32 v21, v25
	v_cvt_pkrtz_f16_f32 v50, v50, v51
	v_cvt_pkrtz_f16_f32 v51, v52, v53
	v_exp_f32_e32 v52, v54
	v_exp_f32_e32 v53, v55
	v_exp_f32_e32 v54, v56
	v_exp_f32_e32 v55, v57
	v_exp_f32_e32 v56, v58
	v_exp_f32_e32 v57, v59
	v_exp_f32_e32 v58, v60
	v_exp_f32_e32 v59, v61
	v_cvt_pkrtz_f16_f32 v44, v18, v19
	v_cvt_pkrtz_f16_f32 v45, v20, v21
	ds_read_b128 v[18:21], v113
	v_exp_f32_e32 v22, v26
	v_exp_f32_e32 v23, v27
	v_cvt_pkrtz_f16_f32 v52, v52, v53
	v_cvt_pkrtz_f16_f32 v53, v54, v55
	v_cvt_pkrtz_f16_f32 v54, v56, v57
	v_cvt_pkrtz_f16_f32 v55, v58, v59
	v_exp_f32_e32 v56, v62
	v_exp_f32_e32 v57, v63
	v_exp_f32_e32 v58, v64
	v_exp_f32_e32 v59, v65
	v_exp_f32_e32 v24, v28
	v_exp_f32_e32 v25, v29
	v_cvt_pkrtz_f16_f32 v46, v22, v23
	v_exp_f32_e32 v48, v30
	v_exp_f32_e32 v49, v31
	v_cvt_pkrtz_f16_f32 v56, v56, v57
	v_cvt_pkrtz_f16_f32 v57, v58, v59
	v_exp_f32_e32 v62, v32
	ds_read_b128 v[58:61], v113 offset:32
	v_cvt_pkrtz_f16_f32 v47, v24, v25
	v_exp_f32_e32 v63, v33
	s_waitcnt lgkmcnt(1)
	v_mfma_f32_32x32x16_f16 v[18:33], v[18:21], v[50:53], 0
	v_cvt_pkrtz_f16_f32 v48, v48, v49
	v_cvt_pkrtz_f16_f32 v49, v62, v63
	ds_read_b128 v[62:65], v113 offset:64
	v_exp_f32_e32 v67, v2
	v_exp_f32_e32 v68, v3
	s_waitcnt lgkmcnt(1)
	v_mfma_f32_32x32x16_f16 v[18:33], v[58:61], v[54:57], v[18:33]
	v_exp_f32_e32 v59, v4
	v_exp_f32_e32 v60, v5
	v_exp_f32_e32 v61, v6
	ds_read_b128 v[2:5], v113 offset:96
	s_waitcnt lgkmcnt(1)
	v_mfma_f32_32x32x16_f16 v[18:33], v[62:65], v[34:37], v[18:33]
	v_exp_f32_e32 v62, v7
	v_exp_f32_e32 v63, v8
	v_exp_f32_e32 v64, v9
	ds_read_b128 v[6:9], v113 offset:128
	s_waitcnt lgkmcnt(1)
	v_mfma_f32_32x32x16_f16 v[18:33], v[2:5], v[38:41], v[18:33]
	v_exp_f32_e32 v10, v10
	ds_read_b128 v[2:5], v113 offset:160
	v_cvt_pkrtz_f16_f32 v58, v67, v68
	v_cvt_pkrtz_f16_f32 v59, v59, v60
	v_cvt_pkrtz_f16_f32 v60, v61, v62
	v_cvt_pkrtz_f16_f32 v61, v63, v64
	s_waitcnt lgkmcnt(1)
	v_mfma_f32_32x32x16_f16 v[18:33], v[6:9], v[42:45], v[18:33]
	v_exp_f32_e32 v11, v11
	v_exp_f32_e32 v12, v12
	v_exp_f32_e32 v13, v13
	ds_read_b128 v[6:9], v113 offset:192
	s_waitcnt lgkmcnt(1)
	v_mfma_f32_32x32x16_f16 v[18:33], v[2:5], v[46:49], v[18:33]
	v_exp_f32_e32 v14, v14
	v_exp_f32_e32 v15, v15
	v_exp_f32_e32 v16, v16
	ds_read_b128 v[2:5], v113 offset:224
	s_waitcnt lgkmcnt(1)
	v_mfma_f32_32x32x16_f16 v[18:33], v[6:9], v[58:61], v[18:33]
	v_exp_f32_e32 v6, v17
	v_cvt_pkrtz_f16_f32 v62, v10, v11
	v_cvt_pkrtz_f16_f32 v63, v12, v13
	v_cvt_pkrtz_f16_f32 v64, v14, v15
	v_cvt_pkrtz_f16_f32 v65, v16, v6
	ds_read_b128 v[6:9], v113 offset:8704
	ds_read_b128 v[66:69], v113 offset:8736
	s_waitcnt lgkmcnt(2)
	v_mfma_f32_32x32x16_f16 v[18:33], v[2:5], v[62:65], v[18:33]
	v_mov_b32_e32 v70, 0
	v_dot2c_f32_f16_e32 v70, 0x3c003c00, v50
	v_dot2c_f32_f16_e32 v70, 0x3c003c00, v51
	v_dot2c_f32_f16_e32 v70, 0x3c003c00, v52
	v_dot2c_f32_f16_e32 v70, 0x3c003c00, v53
	v_dot2c_f32_f16_e32 v70, 0x3c003c00, v54
	v_dot2c_f32_f16_e32 v70, 0x3c003c00, v55
	s_waitcnt lgkmcnt(1)
	v_mfma_f32_32x32x16_f16 v[2:17], v[6:9], v[50:53], 0
	ds_read_b128 v[50:53], v113 offset:8768
	v_dot2c_f32_f16_e32 v70, 0x3c003c00, v56
	v_dot2c_f32_f16_e32 v70, 0x3c003c00, v57
	v_dot2c_f32_f16_e32 v70, 0x3c003c00, v34
	v_dot2c_f32_f16_e32 v70, 0x3c003c00, v35
	v_dot2c_f32_f16_e32 v70, 0x3c003c00, v36
	v_dot2c_f32_f16_e32 v70, 0x3c003c00, v37
	s_waitcnt lgkmcnt(1)
	v_mfma_f32_32x32x16_f16 v[2:17], v[66:69], v[54:57], v[2:17]
	ds_read_b128 v[54:57], v113 offset:8800
	v_dot2c_f32_f16_e32 v70, 0x3c003c00, v38
	v_dot2c_f32_f16_e32 v70, 0x3c003c00, v39
	v_dot2c_f32_f16_e32 v70, 0x3c003c00, v40
	v_dot2c_f32_f16_e32 v70, 0x3c003c00, v41
	v_dot2c_f32_f16_e32 v70, 0x3c003c00, v42
	v_dot2c_f32_f16_e32 v70, 0x3c003c00, v43
	s_waitcnt lgkmcnt(1)
	v_mfma_f32_32x32x16_f16 v[2:17], v[50:53], v[34:37], v[2:17]
	v_dot2c_f32_f16_e32 v70, 0x3c003c00, v44
	ds_read_b128 v[34:37], v113 offset:8832
	v_dot2c_f32_f16_e32 v70, 0x3c003c00, v45
	v_dot2c_f32_f16_e32 v70, 0x3c003c00, v46
	v_dot2c_f32_f16_e32 v70, 0x3c003c00, v47
	v_dot2c_f32_f16_e32 v70, 0x3c003c00, v48
	v_dot2c_f32_f16_e32 v70, 0x3c003c00, v49
	s_waitcnt lgkmcnt(1)
	v_mfma_f32_32x32x16_f16 v[2:17], v[54:57], v[38:41], v[2:17]
	v_dot2c_f32_f16_e32 v70, 0x3c003c00, v58
	v_dot2c_f32_f16_e32 v70, 0x3c003c00, v59
	v_dot2c_f32_f16_e32 v70, 0x3c003c00, v60
	ds_read_b128 v[38:41], v113 offset:8864
	v_dot2c_f32_f16_e32 v70, 0x3c003c00, v61
	v_dot2c_f32_f16_e32 v70, 0x3c003c00, v62
	v_dot2c_f32_f16_e32 v70, 0x3c003c00, v63
	s_waitcnt lgkmcnt(1)
	v_mfma_f32_32x32x16_f16 v[2:17], v[34:37], v[42:45], v[2:17]
	v_dot2c_f32_f16_e32 v70, 0x3c003c00, v64
	v_dot2c_f32_f16_e32 v70, 0x3c003c00, v65
	s_nop 2
	v_mov_b32_e32 v34, v70
	v_mov_b32_e32 v35, v70
	s_nop 1
	v_permlane32_swap_b32_e32 v34, v35
	v_cndmask_b32_e64 v42, v34, v35, s[2:3]
	ds_read_b128 v[34:37], v113 offset:8896
	s_waitcnt lgkmcnt(1)
	v_mfma_f32_32x32x16_f16 v[2:17], v[38:41], v[46:49], v[2:17]
	v_add_f32_e32 v38, v70, v42
	v_rcp_f32_e32 v42, v38
	ds_read_b128 v[38:41], v113 offset:8928
	v_fma_f32 v78, v42, v18, v74
	v_fma_f32 v79, v42, v19, v75
	v_fma_f32 v80, v42, v20, v76
	v_fma_f32 v81, v42, v21, v77
	s_waitcnt lgkmcnt(1)
	v_mfma_f32_32x32x16_f16 v[2:17], v[34:37], v[58:61], v[2:17]
	v_fma_f32 v82, v42, v22, v82
	v_fma_f32 v83, v42, v23, v83
	v_fma_f32 v84, v42, v24, v84
	v_fma_f32 v85, v42, v25, v85
	v_fma_f32 v86, v42, v26, v86
	v_fma_f32 v87, v42, v27, v87
	v_fma_f32 v88, v42, v28, v88
	v_fma_f32 v89, v42, v29, v89
	v_fma_f32 v72, v42, v30, v94
	v_fma_f32 v73, v42, v31, v95
	v_fma_f32 v74, v42, v32, v110
	v_fma_f32 v75, v42, v33, v111
	s_waitcnt lgkmcnt(0)
	v_mfma_f32_32x32x16_f16 v[2:17], v[38:41], v[62:65], v[2:17]
	s_nop 11
	v_fma_f32 v76, v42, v2, v108
	v_fma_f32 v77, v42, v3, v109
	v_fma_f32 v68, v42, v4, v106
	v_fma_f32 v69, v42, v5, v107
	v_fma_f32 v70, v42, v6, v104
	v_fma_f32 v71, v42, v7, v105
	v_pk_fma_f32 v[58:59], v[42:43], v[8:9], v[100:101] op_sel_hi:[0,1,1]
	v_pk_fma_f32 v[66:67], v[42:43], v[10:11], v[96:97] op_sel_hi:[0,1,1]
	v_pk_fma_f32 v[60:61], v[42:43], v[12:13], v[92:93] op_sel_hi:[0,1,1]
	v_pk_fma_f32 v[62:63], v[42:43], v[14:15], v[90:91] op_sel_hi:[0,1,1]
	v_pk_fma_f32 v[64:65], v[42:43], v[16:17], v[102:103] op_sel_hi:[0,1,1]
	v_lshl_add_u64 v[2:3], v[118:119], 1, s[4:5]
	v_lshl_add_u64 v[2:3], v[2:3], 0, v[98:99]
	v_cvt_pk_f16_f32 v5, v80, v81
	v_cvt_pk_f16_f32 v4, v78, v79
	s_waitcnt vmcnt(0)
	s_barrier
	global_store_dwordx2 v[2:3], v[4:5], off
	v_cvt_pk_f16_f32 v5, v84, v85
	v_cvt_pk_f16_f32 v4, v82, v83
	global_store_dwordx2 v[2:3], v[4:5], off offset:16
	v_cvt_pk_f16_f32 v5, v88, v89
	v_cvt_pk_f16_f32 v4, v86, v87
	global_store_dwordx2 v[2:3], v[4:5], off offset:32
	v_cvt_pk_f16_f32 v5, v74, v75
	v_cvt_pk_f16_f32 v4, v72, v73
	global_store_dwordx2 v[2:3], v[4:5], off offset:48
	v_cvt_pk_f16_f32 v5, v68, v69
	v_cvt_pk_f16_f32 v4, v76, v77
	global_store_dwordx2 v[2:3], v[4:5], off offset:64
	v_cvt_pk_f16_f32 v5, v58, v59
	v_cvt_pk_f16_f32 v4, v70, v71
	global_store_dwordx2 v[2:3], v[4:5], off offset:80
	v_cvt_pk_f16_f32 v5, v60, v61
	v_cvt_pk_f16_f32 v4, v66, v67
	global_store_dwordx2 v[2:3], v[4:5], off offset:96
	v_cvt_pk_f16_f32 v5, v64, v65
	v_cvt_pk_f16_f32 v4, v62, v63
	v_cmp_gt_u32_e64 s[0:1], 32, v124
	v_lshl_add_u32 v91, v126, 2, s14
	v_lshl_add_u32 v93, v1, 2, s14
	v_add_u32_e32 v243, 0xfffd8800, v91
	v_add_u32_e32 v242, 0xfffd8800, v93
	s_mov_b64 s[4:5], -1
	v_mov_b32_e32 v95, v78
	v_mov_b32_e32 v94, v79
	v_mov_b32_e32 v97, v80
	v_mov_b32_e32 v96, v81
	v_mov_b32_e32 v99, v82
	v_mov_b32_e32 v98, v83
	v_mov_b32_e32 v35, v84
	v_mov_b32_e32 v34, v85
	v_mov_b32_e32 v37, v86
	v_mov_b32_e32 v36, v87
	v_mov_b32_e32 v39, v88
	v_mov_b32_e32 v38, v89
	v_mov_b32_e32 v41, v72
	v_mov_b32_e32 v40, v73
	v_mov_b32_e32 v19, v74
	v_mov_b32_e32 v18, v75
	v_mov_b32_e32 v21, v76
	v_mov_b32_e32 v20, v77
	v_mov_b32_e32 v23, v68
	v_mov_b32_e32 v22, v69
	v_mov_b32_e32 v42, v70
	v_mov_b32_e32 v24, v71
	v_mov_b32_e32 v43, v58
	v_mov_b32_e32 v27, v59
	v_mov_b32_e32 v26, v66
	v_mov_b32_e32 v25, v67
	v_mov_b32_e32 v29, v60
	v_mov_b32_e32 v28, v61
	v_mov_b32_e32 v32, v62
	v_mov_b32_e32 v30, v63
	v_mov_b32_e32 v33, v64
	v_mov_b32_e32 v31, v65
	global_store_dwordx2 v[2:3], v[4:5], off offset:112
	s_branch .LBB2_95
.LBB2_94:
	s_or_b64 exec, exec, s[14:15]
	s_waitcnt lgkmcnt(0)
	s_barrier
	ds_read_b128 v[244:247], v243
	ds_read_b128 v[6:9], v91
	v_cndmask_b32_e64 v3, v4, v5, s[2:3]
	v_add_f32_e32 v10, v2, v3
	v_mul_f32_e32 v252, 0x3e4ccccd, v10
	v_exp_f32_e32 v10, v10
	v_exp_f32_e32 v252, v252
	ds_read_b128 v[248:251], v243 offset:32
	ds_read_b128 v[2:5], v91 offset:32
	v_mov_b32_e32 v159, 0
	s_waitcnt lgkmcnt(1)
	v_mul_f32_e32 v6, v10, v6
	v_mul_f32_e32 v11, v252, v244
	v_max_f32_e32 v11, v6, v11
	v_mul_f32_e32 v6, v10, v7
	v_mul_f32_e32 v7, v252, v245
	v_max_f32_e32 v12, v6, v7
	v_mul_f32_e32 v6, v10, v8
	v_mul_f32_e32 v7, v252, v246
	v_max_f32_e32 v13, v6, v7
	v_mul_f32_e32 v6, v10, v9
	v_mul_f32_e32 v7, v252, v247
	s_waitcnt lgkmcnt(0)
	v_mul_f32_e32 v2, v10, v2
	v_max_f32_e32 v14, v6, v7
	v_mul_f32_e32 v6, v252, v248
	v_max_f32_e32 v15, v2, v6
	v_mul_f32_e32 v2, v10, v3
	v_mul_f32_e32 v3, v252, v249
	ds_read_b128 v[244:247], v243 offset:64
	ds_read_b128 v[6:9], v91 offset:64
	v_max_f32_e32 v16, v2, v3
	v_mul_f32_e32 v2, v10, v4
	v_mul_f32_e32 v3, v252, v250
	v_max_f32_e32 v17, v2, v3
	v_mul_f32_e32 v2, v10, v5
	v_mul_f32_e32 v3, v252, v251
	v_max_f32_e32 v20, v2, v3
	ds_read_b128 v[248:251], v243 offset:96
	ds_read_b128 v[2:5], v91 offset:96
	s_waitcnt lgkmcnt(1)
	v_mul_f32_e32 v6, v10, v6
	v_mul_f32_e32 v18, v252, v244
	v_max_f32_e32 v22, v6, v18
	v_mul_f32_e32 v6, v10, v7
	v_mul_f32_e32 v7, v252, v245
	v_max_f32_e32 v23, v6, v7
	v_mul_f32_e32 v6, v10, v8
	v_mul_f32_e32 v7, v252, v246
	v_max_f32_e32 v24, v6, v7
	v_mul_f32_e32 v6, v10, v9
	v_mul_f32_e32 v7, v252, v247
	s_waitcnt lgkmcnt(0)
	v_mul_f32_e32 v2, v10, v2
	v_max_f32_e32 v25, v6, v7
	v_mul_f32_e32 v6, v252, v248
	v_max_f32_e32 v26, v2, v6
	v_mul_f32_e32 v2, v10, v3
	v_mul_f32_e32 v3, v252, v249
	ds_read_b128 v[244:247], v243 offset:128
	ds_read_b128 v[6:9], v91 offset:128
	v_max_f32_e32 v27, v2, v3
	v_mul_f32_e32 v2, v10, v4
	v_mul_f32_e32 v3, v252, v250
	v_max_f32_e32 v28, v2, v3
	v_mul_f32_e32 v2, v10, v5
	v_mul_f32_e32 v3, v252, v251
	v_max_f32_e32 v29, v2, v3
	ds_read_b128 v[248:251], v243 offset:160
	ds_read_b128 v[2:5], v91 offset:160
	s_waitcnt lgkmcnt(1)
	v_mul_f32_e32 v6, v10, v6
	v_mul_f32_e32 v18, v252, v244
	v_max_f32_e32 v30, v6, v18
	v_mul_f32_e32 v6, v10, v7
	v_mul_f32_e32 v7, v252, v245
	v_max_f32_e32 v31, v6, v7
	v_mul_f32_e32 v6, v10, v8
	v_mul_f32_e32 v7, v252, v246
	v_max_f32_e32 v32, v6, v7
	v_mul_f32_e32 v6, v10, v9
	v_mul_f32_e32 v7, v252, v247
	s_waitcnt lgkmcnt(0)
	v_mul_f32_e32 v2, v10, v2
	v_max_f32_e32 v33, v6, v7
	v_mul_f32_e32 v6, v252, v248
	v_max_f32_e32 v40, v2, v6
	v_mul_f32_e32 v2, v10, v3
	v_mul_f32_e32 v3, v252, v249
	ds_read_b128 v[244:247], v243 offset:192
	ds_read_b128 v[6:9], v91 offset:192
	v_max_f32_e32 v41, v2, v3
	v_mul_f32_e32 v2, v10, v4
	v_mul_f32_e32 v3, v252, v250
	v_max_f32_e32 v42, v2, v3
	v_mul_f32_e32 v2, v10, v5
	v_mul_f32_e32 v3, v252, v251
	v_max_f32_e32 v43, v2, v3
	ds_read_b128 v[248:251], v243 offset:224
	ds_read_b128 v[2:5], v91 offset:224
	s_waitcnt lgkmcnt(1)
	v_mul_f32_e32 v6, v10, v6
	v_mul_f32_e32 v18, v252, v244
	v_max_f32_e32 v44, v6, v18
	v_mul_f32_e32 v6, v10, v7
	v_mul_f32_e32 v7, v252, v245
	v_max_f32_e32 v45, v6, v7
	v_mul_f32_e32 v6, v10, v8
	v_mul_f32_e32 v7, v252, v246
	v_max_f32_e32 v46, v6, v7
	v_mul_f32_e32 v6, v10, v9
	v_mul_f32_e32 v7, v252, v247
	s_waitcnt lgkmcnt(0)
	v_mul_f32_e32 v2, v10, v2
	v_max_f32_e32 v47, v6, v7
	v_mul_f32_e32 v6, v252, v248
	v_max_f32_e32 v48, v2, v6
	v_mul_f32_e32 v2, v10, v3
	v_mul_f32_e32 v3, v252, v249
	ds_read_b128 v[244:247], v243 offset:256
	ds_read_b128 v[6:9], v91 offset:256
	v_max_f32_e32 v49, v2, v3
	v_mul_f32_e32 v2, v10, v4
	v_mul_f32_e32 v3, v252, v250
	v_max_f32_e32 v50, v2, v3
	v_mul_f32_e32 v2, v10, v5
	v_mul_f32_e32 v3, v252, v251
	v_max_f32_e32 v51, v2, v3
	ds_read_b128 v[248:251], v243 offset:288
	ds_read_b128 v[2:5], v91 offset:288
	s_waitcnt lgkmcnt(1)
	v_mul_f32_e32 v6, v10, v6
	v_mul_f32_e32 v18, v252, v244
	v_max_f32_e32 v52, v6, v18
	v_mul_f32_e32 v6, v10, v7
	v_mul_f32_e32 v7, v252, v245
	v_max_f32_e32 v53, v6, v7
	v_mul_f32_e32 v6, v10, v8
	v_mul_f32_e32 v7, v252, v246
	v_max_f32_e32 v54, v6, v7
	v_mul_f32_e32 v6, v10, v9
	v_mul_f32_e32 v7, v252, v247
	s_waitcnt lgkmcnt(0)
	v_mul_f32_e32 v2, v10, v2
	v_max_f32_e32 v55, v6, v7
	v_mul_f32_e32 v6, v252, v248
	v_max_f32_e32 v56, v2, v6
	v_mul_f32_e32 v2, v10, v3
	v_mul_f32_e32 v3, v252, v249
	ds_read_b128 v[244:247], v243 offset:320
	ds_read_b128 v[6:9], v91 offset:320
	v_max_f32_e32 v57, v2, v3
	v_mul_f32_e32 v2, v10, v4
	v_mul_f32_e32 v3, v252, v250
	v_max_f32_e32 v92, v2, v3
	v_mul_f32_e32 v2, v10, v5
	v_mul_f32_e32 v3, v252, v251
	v_max_f32_e32 v94, v2, v3
	ds_read_b128 v[248:251], v243 offset:352
	ds_read_b128 v[2:5], v91 offset:352
	s_waitcnt lgkmcnt(1)
	v_mul_f32_e32 v6, v10, v6
	v_mul_f32_e32 v18, v252, v244
	v_max_f32_e32 v95, v6, v18
	v_mul_f32_e32 v6, v10, v7
	v_mul_f32_e32 v7, v252, v245
	v_max_f32_e32 v96, v6, v7
	v_mul_f32_e32 v6, v10, v8
	v_mul_f32_e32 v7, v252, v246
	v_max_f32_e32 v97, v6, v7
	v_mul_f32_e32 v6, v10, v9
	v_mul_f32_e32 v7, v252, v247
	s_waitcnt lgkmcnt(0)
	v_mul_f32_e32 v2, v10, v2
	v_max_f32_e32 v98, v6, v7
	v_mul_f32_e32 v6, v252, v248
	v_max_f32_e32 v99, v2, v6
	v_mul_f32_e32 v2, v10, v3
	v_mul_f32_e32 v3, v252, v249
	ds_read_b128 v[244:247], v243 offset:384
	ds_read_b128 v[6:9], v91 offset:384
	v_max_f32_e32 v100, v2, v3
	v_mul_f32_e32 v2, v10, v4
	v_mul_f32_e32 v3, v252, v250
	v_max_f32_e32 v101, v2, v3
	v_mul_f32_e32 v2, v10, v5
	v_mul_f32_e32 v3, v252, v251
	v_max_f32_e32 v102, v2, v3
	ds_read_b128 v[248:251], v243 offset:416
	ds_read_b128 v[2:5], v91 offset:416
	s_waitcnt lgkmcnt(1)
	v_mul_f32_e32 v6, v10, v6
	v_mul_f32_e32 v18, v252, v244
	v_max_f32_e32 v103, v6, v18
	v_mul_f32_e32 v6, v10, v7
	v_mul_f32_e32 v7, v252, v245
	v_max_f32_e32 v104, v6, v7
	v_mul_f32_e32 v6, v10, v8
	v_mul_f32_e32 v7, v252, v246
	v_max_f32_e32 v105, v6, v7
	v_mul_f32_e32 v6, v10, v9
	v_mul_f32_e32 v7, v252, v247
	s_waitcnt lgkmcnt(0)
	v_mul_f32_e32 v2, v10, v2
	v_max_f32_e32 v106, v6, v7
	v_mul_f32_e32 v6, v252, v248
	v_max_f32_e32 v107, v2, v6
	v_mul_f32_e32 v2, v10, v3
	v_mul_f32_e32 v3, v252, v249
	ds_read_b128 v[244:247], v243 offset:448
	ds_read_b128 v[6:9], v91 offset:448
	v_max_f32_e32 v108, v2, v3
	v_mul_f32_e32 v2, v10, v4
	v_mul_f32_e32 v3, v252, v250
	v_max_f32_e32 v109, v2, v3
	v_mul_f32_e32 v2, v10, v5
	v_mul_f32_e32 v3, v252, v251
	v_max_f32_e32 v110, v2, v3
	ds_read_b128 v[248:251], v243 offset:480
	ds_read_b128 v[2:5], v91 offset:480
	s_waitcnt lgkmcnt(1)
	v_mul_f32_e32 v6, v10, v6
	v_mul_f32_e32 v18, v252, v244
	v_max_f32_e32 v111, v6, v18
	v_mul_f32_e32 v6, v10, v7
	v_mul_f32_e32 v7, v252, v245
	v_max_f32_e32 v114, v6, v7
	v_mul_f32_e32 v6, v10, v8
	v_mul_f32_e32 v7, v252, v246
	v_max_f32_e32 v115, v6, v7
	v_mul_f32_e32 v6, v10, v9
	v_mul_f32_e32 v7, v252, v247
	s_waitcnt lgkmcnt(0)
	v_mul_f32_e32 v2, v10, v2
	v_max_f32_e32 v116, v6, v7
	v_mul_f32_e32 v6, v252, v248
	v_max_f32_e32 v117, v2, v6
	v_mul_f32_e32 v2, v10, v3
	v_mul_f32_e32 v3, v252, v249
	v_max_f32_e32 v120, v2, v3
	v_mul_f32_e32 v2, v10, v4
	v_mul_f32_e32 v3, v252, v250
	v_max_f32_e32 v121, v2, v3
	v_mul_f32_e32 v2, v10, v5
	v_mul_f32_e32 v3, v252, v251
	v_max_f32_e32 v122, v2, v3
	s_nop 1
	v_cvt_pkrtz_f16_f32 v2, v11, v12
	v_and_b32_e32 v18, v127, v2
	v_mov_b32_e32 v5, v20
	v_cvt_pkrtz_f16_f32 v2, v13, v14
	v_and_b32_e32 v19, v128, v2
	v_dot2c_f32_f16_e32 v159, 0x3c003c00, v18
	v_cvt_pkrtz_f16_f32 v2, v15, v16
	v_and_b32_e32 v20, v129, v2
	v_cvt_pkrtz_f16_f32 v2, v17, v5
	v_and_b32_e32 v21, v130, v2
	v_cvt_pkrtz_f16_f32 v2, v22, v23
	v_and_b32_e32 v34, v131, v2
	v_cvt_pkrtz_f16_f32 v2, v24, v25
	v_and_b32_e32 v35, v132, v2
	v_cvt_pkrtz_f16_f32 v2, v26, v27
	v_and_b32_e32 v36, v133, v2
	v_cvt_pkrtz_f16_f32 v2, v28, v29
	v_and_b32_e32 v37, v134, v2
	v_cvt_pkrtz_f16_f32 v2, v30, v31
	v_and_b32_e32 v38, v135, v2
	v_cvt_pkrtz_f16_f32 v2, v32, v33
	v_and_b32_e32 v39, v136, v2
	v_cvt_pkrtz_f16_f32 v2, v40, v41
	v_and_b32_e32 v40, v137, v2
	v_cvt_pkrtz_f16_f32 v2, v42, v43
	v_and_b32_e32 v41, v138, v2
	v_cvt_pkrtz_f16_f32 v2, v44, v45
	v_and_b32_e32 v42, v139, v2
	v_cvt_pkrtz_f16_f32 v2, v46, v47
	v_and_b32_e32 v43, v140, v2
	v_cvt_pkrtz_f16_f32 v2, v48, v49
	v_and_b32_e32 v44, v141, v2
	v_cvt_pkrtz_f16_f32 v2, v50, v51
	v_and_b32_e32 v45, v142, v2
	v_cvt_pkrtz_f16_f32 v2, v52, v53
	v_and_b32_e32 v46, v143, v2
	v_cvt_pkrtz_f16_f32 v2, v54, v55
	v_and_b32_e32 v47, v144, v2
	v_cvt_pkrtz_f16_f32 v2, v56, v57
	v_and_b32_e32 v48, v145, v2
	v_cvt_pkrtz_f16_f32 v2, v92, v94
	v_and_b32_e32 v49, v146, v2
	v_cvt_pkrtz_f16_f32 v2, v95, v96
	v_and_b32_e32 v50, v147, v2
	v_cvt_pkrtz_f16_f32 v2, v97, v98
	v_and_b32_e32 v51, v148, v2
	v_cvt_pkrtz_f16_f32 v2, v99, v100
	v_and_b32_e32 v52, v149, v2
	v_cvt_pkrtz_f16_f32 v2, v101, v102
	v_and_b32_e32 v53, v150, v2
	v_cvt_pkrtz_f16_f32 v2, v103, v104
	v_and_b32_e32 v54, v151, v2
	v_cvt_pkrtz_f16_f32 v2, v105, v106
	v_and_b32_e32 v55, v152, v2
	ds_read_b128 v[2:5], v113
	ds_read_b128 v[22:25], v113 offset:32
	s_waitcnt lgkmcnt(1)
	v_mfma_f32_32x32x16_f16 v[2:17], v[2:5], v[18:21], 0
	v_cvt_pkrtz_f16_f32 v26, v107, v108
	v_and_b32_e32 v56, v153, v26
	v_dot2c_f32_f16_e32 v159, 0x3c003c00, v19
	v_cvt_pkrtz_f16_f32 v30, v109, v110
	ds_read_b128 v[26:29], v113 offset:64
	s_waitcnt lgkmcnt(1)
	v_mfma_f32_32x32x16_f16 v[2:17], v[22:25], v[34:37], v[2:17]
	v_and_b32_e32 v57, v154, v30
	ds_read_b128 v[22:25], v113 offset:96
	v_dot2c_f32_f16_e32 v159, 0x3c003c00, v20
	s_waitcnt lgkmcnt(1)
	v_mfma_f32_32x32x16_f16 v[2:17], v[26:29], v[38:41], v[2:17]
	v_cvt_pkrtz_f16_f32 v26, v111, v114
	v_and_b32_e32 v100, v155, v26
	ds_read_b128 v[26:29], v113 offset:128
	s_waitcnt lgkmcnt(1)
	v_mfma_f32_32x32x16_f16 v[2:17], v[22:25], v[42:45], v[2:17]
	v_dot2c_f32_f16_e32 v159, 0x3c003c00, v21
	v_dot2c_f32_f16_e32 v159, 0x3c003c00, v34
	v_dot2c_f32_f16_e32 v159, 0x3c003c00, v35
	v_cvt_pkrtz_f16_f32 v22, v115, v116
	v_dot2c_f32_f16_e32 v159, 0x3c003c00, v36
	v_and_b32_e32 v101, v156, v22
	v_dot2c_f32_f16_e32 v159, 0x3c003c00, v37
	ds_read_b128 v[22:25], v113 offset:160
	v_dot2c_f32_f16_e32 v159, 0x3c003c00, v38
	s_waitcnt lgkmcnt(1)
	v_mfma_f32_32x32x16_f16 v[2:17], v[26:29], v[46:49], v[2:17]
	v_dot2c_f32_f16_e32 v159, 0x3c003c00, v39
	v_dot2c_f32_f16_e32 v159, 0x3c003c00, v40
	v_dot2c_f32_f16_e32 v159, 0x3c003c00, v41
	v_dot2c_f32_f16_e32 v159, 0x3c003c00, v42
	v_dot2c_f32_f16_e32 v159, 0x3c003c00, v43
	v_dot2c_f32_f16_e32 v159, 0x3c003c00, v44
	v_dot2c_f32_f16_e32 v159, 0x3c003c00, v45
	ds_read_b128 v[26:29], v113 offset:192
	v_dot2c_f32_f16_e32 v159, 0x3c003c00, v46
	s_waitcnt lgkmcnt(1)
	v_mfma_f32_32x32x16_f16 v[2:17], v[22:25], v[50:53], v[2:17]
	v_dot2c_f32_f16_e32 v159, 0x3c003c00, v47
	v_dot2c_f32_f16_e32 v159, 0x3c003c00, v48
	v_dot2c_f32_f16_e32 v159, 0x3c003c00, v49
	v_dot2c_f32_f16_e32 v159, 0x3c003c00, v50
	v_dot2c_f32_f16_e32 v159, 0x3c003c00, v51
	v_cvt_pkrtz_f16_f32 v22, v117, v120
	v_dot2c_f32_f16_e32 v159, 0x3c003c00, v52
	v_and_b32_e32 v102, v157, v22
	v_cvt_pkrtz_f16_f32 v22, v121, v122
	v_dot2c_f32_f16_e32 v159, 0x3c003c00, v53
	v_and_b32_e32 v103, v158, v22
	ds_read_b128 v[22:25], v113 offset:224
	v_dot2c_f32_f16_e32 v159, 0x3c003c00, v54
	s_waitcnt lgkmcnt(1)
	v_mfma_f32_32x32x16_f16 v[2:17], v[26:29], v[54:57], v[2:17]
	v_dot2c_f32_f16_e32 v159, 0x3c003c00, v55
	v_dot2c_f32_f16_e32 v159, 0x3c003c00, v56
	v_dot2c_f32_f16_e32 v159, 0x3c003c00, v57
	v_dot2c_f32_f16_e32 v159, 0x3c003c00, v100
	v_dot2c_f32_f16_e32 v159, 0x3c003c00, v101
	v_dot2c_f32_f16_e32 v159, 0x3c003c00, v102
	v_dot2c_f32_f16_e32 v159, 0x3c003c00, v103
	s_waitcnt lgkmcnt(0)
	v_mfma_f32_32x32x16_f16 v[2:17], v[22:25], v[100:103], v[2:17]
	s_xor_b64 s[14:15], s[4:5], -1
	s_mov_b32 s17, 1
	v_mov_b32_e32 v26, v159
	v_mov_b32_e32 v27, v159
	s_nop 1
	v_permlane32_swap_b32_e32 v26, v27
	v_cndmask_b32_e64 v26, v26, v27, s[2:3]
	v_add_f32_e32 v26, v159, v26
	v_rcp_f32_e32 v92, v26
	s_mov_b64 s[4:5], 0
	s_nop 0
	v_pk_mul_f32 v[2:3], v[92:93], v[2:3] op_sel_hi:[0,1]
	v_mul_f32_e32 v22, 0x3fb8aa3b, v2
	v_mul_f32_e32 v23, 0x3fb8aa3b, v3
	v_exp_f32_e32 v22, v22
	v_exp_f32_e32 v23, v23
	v_pk_mul_f32 v[24:25], v[92:93], v[4:5] op_sel_hi:[0,1]
	v_mul_f32_e32 v4, 0x3fb8aa3b, v24
	v_mul_f32_e32 v5, 0x3fb8aa3b, v25
	v_pk_add_f32 v[22:23], v[22:23], -1.0 op_sel_hi:[1,0]
	v_exp_f32_e32 v4, v4
	v_exp_f32_e32 v5, v5
	v_pk_mul_f32 v[104:105], v[92:93], v[6:7] op_sel_hi:[0,1]
	v_pk_mul_f32 v[108:109], v[92:93], v[8:9] op_sel_hi:[0,1]
	v_med3_f32 v94, v3, v23, 0
	v_pk_mul_f32 v[10:11], v[92:93], v[10:11] op_sel_hi:[0,1]
	v_pk_mul_f32 v[12:13], v[92:93], v[12:13] op_sel_hi:[0,1]
	v_med3_f32 v95, v2, v22, 0
	v_mul_f32_e32 v2, 0x3fb8aa3b, v104
	v_exp_f32_e32 v6, v2
	v_mul_f32_e32 v2, 0x3fb8aa3b, v105
	v_pk_add_f32 v[22:23], v[4:5], -1.0 op_sel_hi:[1,0]
	v_exp_f32_e32 v7, v2
	ds_read_b128 v[2:5], v113 offset:8704
	v_pk_mul_f32 v[14:15], v[92:93], v[14:15] op_sel_hi:[0,1]
	v_pk_add_f32 v[106:107], v[6:7], -1.0 op_sel_hi:[1,0]
	v_mul_f32_e32 v6, 0x3fb8aa3b, v108
	v_med3_f32 v96, v25, v23, 0
	v_exp_f32_e32 v110, v6
	ds_read_b128 v[6:9], v113 offset:8736
	v_med3_f32 v97, v24, v22, 0
	s_waitcnt lgkmcnt(1)
	v_mfma_f32_32x32x16_f16 v[18:33], v[2:5], v[18:21], 0
	v_mul_f32_e32 v2, 0x3fb8aa3b, v109
	v_exp_f32_e32 v111, v2
	ds_read_b128 v[2:5], v113 offset:8768
	v_med3_f32 v98, v105, v107, 0
	s_waitcnt lgkmcnt(1)
	v_mfma_f32_32x32x16_f16 v[18:33], v[6:9], v[34:37], v[18:33]
	v_mul_f32_e32 v6, 0x3fb8aa3b, v10
	v_exp_f32_e32 v36, v6
	v_mul_f32_e32 v6, 0x3fb8aa3b, v11
	v_exp_f32_e32 v37, v6
	ds_read_b128 v[6:9], v113 offset:8800
	v_cmp_lt_f32_e32 vcc, 0, v104
	s_waitcnt lgkmcnt(1)
	v_mfma_f32_32x32x16_f16 v[18:33], v[2:5], v[38:41], v[18:33]
	v_mul_f32_e32 v2, 0x3fb8aa3b, v12
	v_exp_f32_e32 v40, v2
	ds_read_b128 v[2:5], v113 offset:8832
	v_add_f32_e32 v38, -1.0, v36
	v_add_f32_e32 v39, -1.0, v37
	v_mul_f32_e32 v36, 0x3fb8aa3b, v13
	v_cndmask_b32_e32 v99, v106, v104, vcc
	v_add_f32_e32 v104, -1.0, v110
	v_add_f32_e32 v105, -1.0, v111
	s_waitcnt lgkmcnt(1)
	v_mfma_f32_32x32x16_f16 v[18:33], v[6:9], v[42:45], v[18:33]
	ds_read_b128 v[6:9], v113 offset:8864
	v_exp_f32_e32 v41, v36
	v_med3_f32 v34, v109, v105, 0
	s_waitcnt lgkmcnt(1)
	v_mfma_f32_32x32x16_f16 v[18:33], v[2:5], v[46:49], v[18:33]
	v_med3_f32 v35, v108, v104, 0
	v_mul_f32_e32 v2, 0x3fb8aa3b, v14
	v_med3_f32 v36, v11, v39, 0
	s_waitcnt lgkmcnt(0)
	v_mfma_f32_32x32x16_f16 v[18:33], v[6:9], v[50:53], v[18:33]
	v_med3_f32 v37, v10, v38, 0
	v_add_f32_e64 v10, v40, -1.0
	v_add_f32_e64 v11, v41, -1.0
	v_exp_f32_e32 v40, v2
	v_mul_f32_e32 v2, 0x3fb8aa3b, v15
	v_exp_f32_e32 v41, v2
	ds_read_b128 v[2:5], v113 offset:8896
	v_med3_f32 v38, v13, v11, 0
	v_med3_f32 v39, v12, v10, 0
	v_pk_mul_f32 v[12:13], v[92:93], v[16:17] op_sel_hi:[0,1]
	v_mul_f32_e32 v6, 0x3fb8aa3b, v12
	v_exp_f32_e32 v16, v6
	ds_read_b128 v[6:9], v113 offset:8928
	s_waitcnt lgkmcnt(1)
	v_mfma_f32_32x32x16_f16 v[18:33], v[2:5], v[54:57], v[18:33]
	v_mul_f32_e32 v2, 0x3fb8aa3b, v13
	v_exp_f32_e32 v17, v2
	v_add_f32_e32 v10, -1.0, v40
	v_add_f32_e32 v11, -1.0, v41
	s_waitcnt lgkmcnt(0)
	v_add_f32_e32 v2, -1.0, v16
	v_add_f32_e32 v3, -1.0, v17
	v_med3_f32 v40, v15, v11, 0
	v_mfma_f32_32x32x16_f16 v[18:33], v[6:9], v[100:103], v[18:33]
	s_barrier
	v_med3_f32 v41, v14, v10, 0
	s_nop 9
	v_pk_mul_f32 v[4:5], v[92:93], v[18:19] op_sel_hi:[0,1]
	v_mul_f32_e32 v6, 0x3fb8aa3b, v4
	v_mul_f32_e32 v7, 0x3fb8aa3b, v5
	v_exp_f32_e32 v6, v6
	v_exp_f32_e32 v7, v7
	s_nop 4
	v_med3_f32 v18, v13, v3, 0
	s_nop 3
	v_med3_f32 v19, v12, v2, 0
	v_pk_add_f32 v[2:3], v[6:7], -1.0 op_sel_hi:[1,0]
	s_nop 1
	v_pk_mul_f32 v[6:7], v[92:93], v[20:21] op_sel_hi:[0,1]
	v_mul_f32_e32 v8, 0x3fb8aa3b, v6
	v_mul_f32_e32 v9, 0x3fb8aa3b, v7
	v_exp_f32_e32 v8, v8
	v_exp_f32_e32 v9, v9
	v_med3_f32 v20, v5, v3, 0
	v_med3_f32 v21, v4, v2, 0
	v_pk_mul_f32 v[4:5], v[92:93], v[22:23] op_sel_hi:[0,1]
	v_pk_add_f32 v[2:3], v[8:9], -1.0 op_sel_hi:[1,0]
	v_mul_f32_e32 v8, 0x3fb8aa3b, v4
	v_mul_f32_e32 v9, 0x3fb8aa3b, v5
	v_exp_f32_e32 v8, v8
	v_exp_f32_e32 v9, v9
	v_med3_f32 v22, v7, v3, 0
	v_med3_f32 v23, v6, v2, 0
	v_pk_mul_f32 v[6:7], v[92:93], v[24:25] op_sel_hi:[0,1]
	v_pk_add_f32 v[2:3], v[8:9], -1.0 op_sel_hi:[1,0]
	v_mul_f32_e32 v8, 0x3fb8aa3b, v6
	v_mul_f32_e32 v9, 0x3fb8aa3b, v7
	v_exp_f32_e32 v8, v8
	v_exp_f32_e32 v9, v9
	v_med3_f32 v24, v5, v3, 0
	v_med3_f32 v42, v4, v2, 0
	v_pk_mul_f32 v[4:5], v[92:93], v[26:27] op_sel_hi:[0,1]
	v_pk_add_f32 v[2:3], v[8:9], -1.0 op_sel_hi:[1,0]
	v_mul_f32_e32 v8, 0x3fb8aa3b, v4
	v_mul_f32_e32 v9, 0x3fb8aa3b, v5
	v_exp_f32_e32 v8, v8
	v_exp_f32_e32 v9, v9
	v_med3_f32 v27, v7, v3, 0
	v_med3_f32 v43, v6, v2, 0
	v_pk_mul_f32 v[6:7], v[92:93], v[28:29] op_sel_hi:[0,1]
	v_pk_add_f32 v[2:3], v[8:9], -1.0 op_sel_hi:[1,0]
	v_mul_f32_e32 v8, 0x3fb8aa3b, v6
	v_mul_f32_e32 v9, 0x3fb8aa3b, v7
	v_exp_f32_e32 v8, v8
	v_exp_f32_e32 v9, v9
	v_med3_f32 v25, v5, v3, 0
	v_med3_f32 v26, v4, v2, 0
	v_pk_mul_f32 v[4:5], v[92:93], v[30:31] op_sel_hi:[0,1]
	v_pk_add_f32 v[2:3], v[8:9], -1.0 op_sel_hi:[1,0]
	v_mul_f32_e32 v8, 0x3fb8aa3b, v4
	v_mul_f32_e32 v9, 0x3fb8aa3b, v5
	v_exp_f32_e32 v8, v8
	v_exp_f32_e32 v9, v9
	v_med3_f32 v28, v7, v3, 0
	v_med3_f32 v29, v6, v2, 0
	v_pk_mul_f32 v[6:7], v[92:93], v[32:33] op_sel_hi:[0,1]
	v_pk_add_f32 v[2:3], v[8:9], -1.0 op_sel_hi:[1,0]
	v_mul_f32_e32 v8, 0x3fb8aa3b, v6
	v_mul_f32_e32 v9, 0x3fb8aa3b, v7
	v_exp_f32_e32 v8, v8
	v_exp_f32_e32 v9, v9
	v_med3_f32 v30, v5, v3, 0
	v_med3_f32 v32, v4, v2, 0
	v_pk_add_f32 v[2:3], v[8:9], -1.0 op_sel_hi:[1,0]
	v_med3_f32 v31, v7, v3, 0
	v_med3_f32 v33, v6, v2, 0
	s_and_b64 vcc, exec, s[14:15]
	s_cbranch_vccnz .LBB2_97
.LBB2_95:
	v_lshl_add_u32 v56, s17, 13, v125
	v_cvt_pkrtz_f16_f32 v44, v95, v94
	v_cvt_pkrtz_f16_f32 v45, v97, v96
	v_cvt_pkrtz_f16_f32 v46, v99, v98
	v_cvt_pkrtz_f16_f32 v47, v35, v34
	ds_read_b128 v[2:5], v56 offset:24576
	ds_read_b128 v[52:55], v56 offset:25600
	s_waitcnt lgkmcnt(1)
	v_mfma_f32_32x32x16_f16 v[2:17], v[44:47], v[2:5], 0
	v_cvt_pkrtz_f16_f32 v48, v37, v36
	v_cvt_pkrtz_f16_f32 v49, v39, v38
	v_cvt_pkrtz_f16_f32 v50, v41, v40
	v_cvt_pkrtz_f16_f32 v51, v19, v18
	v_cvt_pkrtz_f16_f32 v100, v21, v20
	v_cvt_pkrtz_f16_f32 v101, v23, v22
	v_cvt_pkrtz_f16_f32 v102, v42, v24
	s_waitcnt lgkmcnt(0)
	v_mfma_f32_32x32x16_f16 v[2:17], v[48:51], v[52:55], v[2:17]
	v_cvt_pkrtz_f16_f32 v103, v43, v27
	ds_read_b128 v[52:55], v56 offset:26624
	ds_read_b128 v[108:111], v56 offset:27648
	v_cvt_pkrtz_f16_f32 v104, v26, v25
	v_cvt_pkrtz_f16_f32 v105, v29, v28
	v_cvt_pkrtz_f16_f32 v106, v32, v30
	v_cvt_pkrtz_f16_f32 v107, v33, v31
	s_waitcnt lgkmcnt(1)
	v_mfma_f32_32x32x16_f16 v[2:17], v[100:103], v[52:55], v[2:17]
	v_lshlrev_b32_e32 v90, 2, v126
	s_waitcnt lgkmcnt(0)
	v_mfma_f32_32x32x16_f16 v[2:17], v[104:107], v[108:111], v[2:17]
	s_nop 11
	v_cvt_pkrtz_f16_f32 v2, v2, v3
	v_cvt_pkrtz_f16_f32 v3, v4, v5
	v_cvt_pkrtz_f16_f32 v4, v6, v7
	v_cvt_pkrtz_f16_f32 v5, v8, v9
	v_cvt_pkrtz_f16_f32 v6, v10, v11
	v_cvt_pkrtz_f16_f32 v7, v12, v13
	v_cvt_pkrtz_f16_f32 v8, v14, v15
	v_cvt_pkrtz_f16_f32 v9, v16, v17
	ds_write_b128 v112, v[2:5]
	ds_write_b128 v112, v[6:9] offset:32
	ds_read_b128 v[2:5], v56 offset:28672
	ds_read_b128 v[52:55], v56 offset:29696
	s_waitcnt lgkmcnt(1)
	v_mfma_f32_32x32x16_f16 v[2:17], v[44:47], v[2:5], 0
	s_waitcnt lgkmcnt(0)
	v_mfma_f32_32x32x16_f16 v[2:17], v[48:51], v[52:55], v[2:17]
	ds_read_b128 v[44:47], v56 offset:30720
	ds_read_b128 v[48:51], v56 offset:31744
	s_waitcnt lgkmcnt(1)
	v_mfma_f32_32x32x16_f16 v[2:17], v[100:103], v[44:47], v[2:17]
	v_lshl_or_b32 v44, s17, 9, v90
	v_add_u32_e32 v56, 0, v44
	s_waitcnt lgkmcnt(0)
	v_mfma_f32_32x32x16_f16 v[2:17], v[104:107], v[48:51], v[2:17]
	s_nop 11
	v_cvt_pkrtz_f16_f32 v2, v2, v3
	v_cvt_pkrtz_f16_f32 v3, v4, v5
	v_cvt_pkrtz_f16_f32 v4, v6, v7
	v_cvt_pkrtz_f16_f32 v5, v8, v9
	v_cvt_pkrtz_f16_f32 v6, v10, v11
	v_cvt_pkrtz_f16_f32 v7, v12, v13
	v_cvt_pkrtz_f16_f32 v8, v14, v15
	v_cvt_pkrtz_f16_f32 v9, v16, v17
	ds_write_b128 v112, v[2:5] offset:8704
	ds_write_b128 v112, v[6:9] offset:8736
	ds_read_b128 v[4:7], v56 offset:61440
	ds_read_b128 v[8:11], v56 offset:61472
	ds_read_b128 v[12:15], v56 offset:61696
	ds_read_b128 v[44:47], v56 offset:61728
	ds_read_b128 v[48:51], v56 offset:61504
	ds_read_b128 v[52:55], v56 offset:61536
	ds_read_b128 v[100:103], v56 offset:61760
	ds_read_b128 v[104:107], v56 offset:61792
	ds_read_b128 v[108:111], v56 offset:61568
	ds_read_b128 v[114:117], v56 offset:61600
	ds_read_b128 v[120:123], v56 offset:61824
	ds_read_b128 v[160:163], v56 offset:61856
	s_waitcnt lgkmcnt(11)
	v_fma_f32 v2, v4, v95, 0
	s_waitcnt lgkmcnt(9)
	v_fma_f32 v3, v12, v95, 0
	v_fmac_f32_e32 v2, v5, v94
	v_fmac_f32_e32 v3, v13, v94
	v_fmac_f32_e32 v2, v6, v97
	v_fmac_f32_e32 v3, v14, v97
	v_fmac_f32_e32 v2, v7, v96
	v_fmac_f32_e32 v3, v15, v96
	v_fmac_f32_e32 v2, v8, v99
	s_waitcnt lgkmcnt(8)
	v_fmac_f32_e32 v3, v44, v99
	v_fmac_f32_e32 v2, v9, v98
	v_fmac_f32_e32 v3, v45, v98
	v_fmac_f32_e32 v2, v10, v35
	v_fmac_f32_e32 v3, v46, v35
	v_fmac_f32_e32 v2, v11, v34
	v_fmac_f32_e32 v3, v47, v34
	s_waitcnt lgkmcnt(7)
	v_fmac_f32_e32 v2, v48, v37
	s_waitcnt lgkmcnt(5)
	v_fmac_f32_e32 v3, v100, v37
	v_fmac_f32_e32 v2, v49, v36
	v_fmac_f32_e32 v3, v101, v36
	v_fmac_f32_e32 v2, v50, v39
	v_fmac_f32_e32 v3, v102, v39
	v_fmac_f32_e32 v2, v51, v38
	v_fmac_f32_e32 v3, v103, v38
	v_fmac_f32_e32 v2, v52, v41
	s_waitcnt lgkmcnt(4)
	v_fmac_f32_e32 v3, v104, v41
	v_fmac_f32_e32 v2, v53, v40
	v_fmac_f32_e32 v3, v105, v40
	v_fmac_f32_e32 v2, v54, v19
	v_fmac_f32_e32 v3, v106, v19
	v_fmac_f32_e32 v2, v55, v18
	v_fmac_f32_e32 v3, v107, v18
	s_waitcnt lgkmcnt(3)
	v_fmac_f32_e32 v2, v108, v21
	s_waitcnt lgkmcnt(1)
	v_fmac_f32_e32 v3, v120, v21
	v_fmac_f32_e32 v2, v109, v20
	v_fmac_f32_e32 v3, v121, v20
	v_fmac_f32_e32 v2, v110, v23
	v_fmac_f32_e32 v3, v122, v23
	v_fmac_f32_e32 v2, v111, v22
	v_fmac_f32_e32 v3, v123, v22
	ds_read_b128 v[4:7], v56 offset:61632
	ds_read_b128 v[12:15], v56 offset:61664
	ds_read_b128 v[8:11], v56 offset:61888
	ds_read_b128 v[16:19], v56 offset:61920
	v_fmac_f32_e32 v2, v114, v42
	s_waitcnt lgkmcnt(4)
	v_fmac_f32_e32 v3, v160, v42
	v_fmac_f32_e32 v2, v115, v24
	v_fmac_f32_e32 v3, v161, v24
	v_fmac_f32_e32 v2, v116, v43
	v_fmac_f32_e32 v3, v162, v43
	v_fmac_f32_e32 v2, v117, v27
	v_fmac_f32_e32 v3, v163, v27
	s_waitcnt lgkmcnt(3)
	v_fmac_f32_e32 v2, v4, v26
	s_waitcnt lgkmcnt(1)
	v_fmac_f32_e32 v3, v8, v26
	v_fmac_f32_e32 v2, v5, v25
	v_fmac_f32_e32 v3, v9, v25
	v_fmac_f32_e32 v2, v6, v29
	v_fmac_f32_e32 v3, v10, v29
	v_fmac_f32_e32 v2, v7, v28
	v_fmac_f32_e32 v3, v11, v28
	v_fmac_f32_e32 v2, v12, v32
	s_waitcnt lgkmcnt(0)
	v_fmac_f32_e32 v3, v16, v32
	v_fmac_f32_e32 v2, v13, v30
	v_fmac_f32_e32 v3, v17, v30
	v_fmac_f32_e32 v2, v14, v33
	v_fmac_f32_e32 v3, v18, v33
	v_fmac_f32_e32 v2, v15, v31
	v_fmac_f32_e32 v3, v19, v31
	v_mov_b32_e32 v4, v2
	v_mov_b32_e32 v5, v2
	v_mov_b32_e32 v6, v3
	v_mov_b32_e32 v7, v3
	v_permlane32_swap_b32_e32 v4, v5
	s_nop 0
	v_permlane32_swap_b32_e32 v6, v7
	s_and_saveexec_b64 s[14:15], s[0:1]
	s_cbranch_execz .LBB2_94
	v_cndmask_b32_e64 v6, v6, v7, s[2:3]
	v_add_f32_e32 v3, v3, v6
	v_mul_f32_e32 v6, 0x3e4ccccd, v3
	v_exp_f32_e32 v3, v3
	v_exp_f32_e32 v6, v6
	s_nop 0
	ds_write_b32 v93, v3
	ds_write_b32 v242, v6
	s_branch .LBB2_94
